# transpose items in two regimes: five-item and KV-tile workers take one item, the lightest workers take three
# speedup vs baseline: 1.0086x; 1.0012x over previous
; __device__ __forceinline__ void late_weight_prep(const Params& P, LAS unsigned char* lds, int lane, int wave, int gw, int NGW) {
;     ...
;         for (int it = gw; it < I_OUT + I_Q + I_O; it += NGW) {
;             int r = it;
;             if (r < I_OUT) { p0_transpose_item(P.w_out, 1024, 1024, 0, 32, (bf16*)(ws + WS_WOUT), 0, nullptr, scr, r, lane); continue; } r -= I_OUT;
;             if (r < I_Q) { p0_transpose_item(P.xattn_wq, 1024, 1024, 0, 32, (bf16*)(ws + WS_WQ), 0, P.norm_xattn_w, scr, r, lane); continue; } r -= I_Q;
;             p0_transpose_item(P.xattn_wo, 1024, 1024, 0, 32, (bf16*)(ws + WS_WO), 0, nullptr, scr, r, lane);
;         }
; __global__ void __launch_bounds__(NWAVES * 64, 2) hybrid_fwd(Params P) {
;     ...
;                 late_weight_prep(P, lds, lane, wave, w2 * NWAVES + wave, N2 * NWAVES);
.LBB0_1975:
	s_ashr_i32 s15, s14, 31
	s_cmpk_lt_i32 s16, 0x400
	s_cbranch_scc1 .LBB0_2008
	v_and_b32_e32 v1, 31, v0
	v_lshlrev_b32_e32 v20, 2, v1
	v_lshlrev_b32_e32 v1, 3, v0
	v_and_b32_e32 v1, 56, v1
	v_readlane_b32 s0, v254, 56
	v_lshlrev_b32_e32 v6, 1, v1
	v_mov_b32_e32 v7, 0
	s_mov_b32 s22, s0
	s_lshl_b32 s0, s0, 14
	v_lshrrev_b32_e32 v23, 3, v182
	v_lshl_add_u64 v[12:13], s[24:25], 0, v[6:7]
	s_mov_b64 s[6:7], 0x1200000
	v_readlane_b32 s44, v254, 40
	s_add_i32 s13, s0, 0
	v_lshrrev_b32_e32 v2, 5, v182
	v_mul_u32_u24_e32 v3, 0x84, v1
	v_lshl_add_u64 v[8:9], v[12:13], 0, s[6:7]
	v_lshlrev_b32_e32 v1, 2, v23
	s_mov_b64 s[6:7], 0xc00000
	v_readlane_b32 s45, v254, 41
	v_add3_u32 v44, s13, v3, v1
	v_lshl_add_u64 v[10:11], v[12:13], 0, s[6:7]
	s_mov_b64 s[6:7], 0xa00000
	s_cmp_lg_u64 s[44:45], 0
	v_mul_u32_u24_e32 v3, 0x84, v2
	v_lshl_add_u64 v[12:13], v[12:13], 0, s[6:7]
	v_mov_b32_e32 v21, v7
	v_readlane_b32 s52, v254, 48
	v_readlane_b32 s53, v254, 49
	v_readlane_b32 s54, v254, 50
	v_readlane_b32 s55, v254, 51
	v_readlane_b32 s56, v254, 52
	v_readlane_b32 s57, v254, 53
	v_readlane_b32 s58, v254, 54
	v_readlane_b32 s59, v254, 55
	s_cselect_b64 s[42:43], -1, 0
	v_or_b32_e32 v3, s0, v3
	s_lshl_b32 s0, s14, 8
	s_lshl_b32 s6, s22, 5
	v_add_u32_e32 v4, s13, v20
	v_lshl_add_u64 v[14:15], s[52:53], 0, v[20:21]
	v_readlane_b32 s52, v254, 24
	s_add_i32 s13, s0, s6
	s_add_i32 s13, s13, 0xffff8000
	s_lshl_b32 s0, s14, 4
	s_lshl_b32 s6, s22, 1
	v_readlane_b32 s1, v254, 57
	v_readlane_b32 s48, v254, 44
	v_readlane_b32 s49, v254, 45
	v_readlane_b32 s66, v254, 38
	v_readlane_b32 s67, v254, 39
	s_lshl_b32 s17, s26, 8
	s_add_i32 s0, s0, s6
	s_lshl_b32 s30, s26, 4
	s_mov_b32 s1, 0
	s_movk_i32 s3, 0x84
	v_or_b32_e32 v45, 8, v23
	v_or_b32_e32 v46, 16, v23
	v_or_b32_e32 v47, 24, v23
	v_lshl_add_u64 v[16:17], s[66:67], 0, v[20:21]
	v_mov_b32_e32 v1, v2
	v_add3_u32 v48, v3, v20, 0
	v_lshl_add_u64 v[20:21], s[48:49], 0, v[20:21]
	s_addk_i32 s17, 0xde00
	v_or_b32_e32 v49, 14, v2
	s_add_i32 s19, s0, 0x1f400
	s_addk_i32 s30, 0xfde0
	v_lshlrev_b32_e32 v22, 2, v2
	v_mov_b32_e32 v3, v7
	v_or_b32_e32 v50, 12, v2
	v_or_b32_e32 v51, 10, v2
	v_or_b32_e32 v52, 8, v2
	v_or_b32_e32 v53, 6, v2
	v_or_b32_e32 v54, 4, v2
	v_or_b32_e32 v55, 2, v2
	s_movk_i32 s31, 0x7fff
	s_mov_b32 s34, 0xffff0000
	s_add_i32 s35, s16, 0xfffffc00
	s_cmpk_lt_i32 s16, 0x570
	s_movk_i32 s99, 0x180
	s_cselect_b32 s98, 0x1000, s99
	s_lshl_b32 s99, s98, 5
	s_lshl_b32 s100, s98, 1
	v_readlane_b32 s46, v254, 42
	v_readlane_b32 s47, v254, 43
	v_readlane_b32 s50, v254, 46
	v_readlane_b32 s51, v254, 47
	v_readlane_b32 s53, v254, 25
	v_readlane_b32 s54, v254, 26
	v_readlane_b32 s55, v254, 27
	v_readlane_b32 s56, v254, 28
	v_readlane_b32 s57, v254, 29
	v_readlane_b32 s58, v254, 30
	v_readlane_b32 s59, v254, 31
	v_readlane_b32 s60, v254, 32
	v_readlane_b32 s61, v254, 33
	v_readlane_b32 s62, v254, 34
	v_readlane_b32 s63, v254, 35
	v_readlane_b32 s64, v254, 36
	v_readlane_b32 s65, v254, 37
	s_branch .LBB0_1978
.LBB0_1977:
	s_add_i32 s35, s35, s98
	s_add_i32 s13, s13, s99
	s_add_i32 s19, s19, s100
	s_cmpk_gt_i32 s35, 0x5ff
	s_cbranch_scc1 .LBB0_2008
